# P0 load rebalancing: GEMV workgroups take 2 weight-conversion items per wave, table workgroups take the rest
# speedup vs baseline: 1.0144x; 1.0094x over previous
.LBB0_41:
	s_or_b64 exec, exec, s[2:3]
	s_lshl_b32 s2, s80, 3
	s_add_i32 s16, s97, s2
	s_lshl_b32 s17, s62, 3
	s_movk_i32 s32, 0x2020
	s_cmpk_lg_i32 s62, 0x100
	s_cbranch_scc1 .Lp0_go
	s_cmpk_lt_u32 s80, 0xc0
	s_cbranch_scc0 .Lp0_tbl
	s_movk_i32 s17, 0x600
	s_movk_i32 s32, 0xc00
	s_branch .Lp0_go
.Lp0_tbl:
	s_addk_i32 s16, 0x600
	s_movk_i32 s17, 0x200
.Lp0_go:
	s_cmp_ge_i32 s16, s32
	s_cbranch_scc1 .LBB0_55
	s_load_dwordx4 s[12:15], s[0:1], 0x120
	v_and_b32_e32 v1, 31, v0
	v_lshlrev_b32_e32 v4, 2, v1
	v_lshlrev_b32_e32 v1, 3, v0
	s_load_dwordx16 s[36:51], s[0:1], 0x40
	v_mov_b32_e32 v5, 0
	v_and_b32_e32 v1, 56, v1
	v_lshlrev_b32_e32 v12, 1, v1
	v_mov_b32_e32 v13, v5
	s_lshl_b32 s2, s97, 14
	s_waitcnt lgkmcnt(0)
	v_lshl_add_u64 v[16:17], s[14:15], 0, v[12:13]
	s_mov_b64 s[6:7], 0x1c00000
	s_add_i32 s2, s2, 0
	v_lshrrev_b32_e32 v3, 3, v206
	v_lshl_add_u64 v[12:13], v[16:17], 0, s[6:7]
	s_mov_b64 s[6:7], 0x300000
	v_and_b32_e32 v25, 28, v6
	v_lshrrev_b32_e32 v2, 5, v206
	v_lshl_add_u64 v[8:9], s[68:69], 0, v[4:5]
	v_add_u32_e32 v10, s2, v4
	v_mul_u32_u24_e32 v7, 0x84, v1
	v_lshlrev_b32_e32 v1, 2, v3
	v_lshl_add_u64 v[14:15], s[36:37], 0, v[4:5]
	v_lshl_add_u64 v[16:17], v[16:17], 0, s[6:7]
	v_lshlrev_b32_e32 v4, 2, v25
	s_add_u32 s6, s14, 0x2df00000
	s_mov_b32 s3, 0
	s_movk_i32 s18, 0x84
	v_add3_u32 v11, s2, v7, v1
	v_or_b32_e32 v22, 8, v3
	v_or_b32_e32 v23, 16, v3
	v_or_b32_e32 v24, 24, v3
	v_and_b32_e32 v18, 56, v0
	v_lshl_add_u64 v[6:7], s[36:37], 0, v[4:5]
	s_addc_u32 s7, s15, 0
	v_mov_b32_e32 v19, v5
	v_mov_b32_e32 v1, v2
	s_movk_i32 s19, 0x6080
	s_mov_b32 s20, 0xc3e00000
	s_movk_i32 s21, 0x1000
	v_mov_b32_e32 v26, 0x43e00000
	s_branch .LBB0_45

.LBB0_44:
	s_add_i32 s16, s16, s17
	s_cmp_lt_i32 s16, s32
	s_cbranch_scc0 .LBB0_55
